# P0 adaLN mat-vec k-loop as a counted double buffer: next trip's 16 weight rows requested before this trip's arithmetic
# speedup vs baseline: 1.0066x; 1.0037x over previous
.LBB0_25:
	s_or_b64 exec, exec, s[8:9]
	s_waitcnt lgkmcnt(0)
	s_barrier
	ds_read_b32 v4, v5 offset:560
	ds_read_b32 v66, v5 offset:564
	s_mul_hi_i32 s6, s93, 0x2aaaaaab
	s_lshr_b32 s7, s6, 31
	s_ashr_i32 s6, s6, 3
	s_add_i32 s20, s6, s7
	s_waitcnt lgkmcnt(0)
	v_readfirstlane_b32 s7, v66
	v_readfirstlane_b32 s6, v4
	s_mul_i32 s21, s20, 0x1800
	s_mul_i32 s9, s20, 0x1800000
	v_lshl_add_u64 v[66:67], s[6:7], 0, v[60:61]
	s_sub_i32 s6, s42, s21
	s_ashr_i32 s7, s6, 31
	s_lshl_b64 s[6:7], s[6:7], 2
	s_mul_hi_i32 s8, s20, 0x1800000
	s_add_u32 s6, s9, s6
	s_addc_u32 s7, s8, s7
	v_lshl_add_u64 v[66:67], v[66:67], 0, s[6:7]
	v_mov_b32_e32 v76, 0
	v_lshl_add_u64 v[66:67], v[66:67], 0, s[66:67]
	s_mov_b32 s6, -16
	s_mov_b32 s7, s92
	v_mov_b32_e32 v70, 0
	v_mov_b32_e32 v71, v76
	v_mov_b32_e32 v68, 0
	v_mov_b32_e32 v69, v76
	v_mov_b32_e32 v72, 0
	v_mov_b32_e32 v73, v76
	v_mov_b32_e32 v74, 0
	v_mov_b32_e32 v75, v76
	s_mov_b32 s8, 0xfffa6000
	v_add_co_u32_e32 v230, vcc, s8, v66
	s_nop 1
	v_addc_co_u32_e32 v231, vcc, -1, v67, vcc
	global_load_dword v214, v[230:231], off
	s_mov_b32 s8, 0xfffac000
	v_add_co_u32_e32 v230, vcc, s8, v66
	s_nop 1
	v_addc_co_u32_e32 v231, vcc, -1, v67, vcc
	global_load_dword v215, v[230:231], off
	s_mov_b32 s8, 0xfffb2000
	v_add_co_u32_e32 v230, vcc, s8, v66
	s_nop 1
	v_addc_co_u32_e32 v231, vcc, -1, v67, vcc
	global_load_dword v216, v[230:231], off
	s_mov_b32 s8, 0xfffb8000
	v_add_co_u32_e32 v230, vcc, s8, v66
	s_nop 1
	v_addc_co_u32_e32 v231, vcc, -1, v67, vcc
	global_load_dword v217, v[230:231], off
	s_mov_b32 s8, 0xfffbe000
	v_add_co_u32_e32 v230, vcc, s8, v66
	s_nop 1
	v_addc_co_u32_e32 v231, vcc, -1, v67, vcc
	global_load_dword v218, v[230:231], off
	s_mov_b32 s8, 0xfffc4000
	v_add_co_u32_e32 v230, vcc, s8, v66
	s_nop 1
	v_addc_co_u32_e32 v231, vcc, -1, v67, vcc
	global_load_dword v219, v[230:231], off
	s_mov_b32 s8, 0xfffca000
	v_add_co_u32_e32 v230, vcc, s8, v66
	s_nop 1
	v_addc_co_u32_e32 v231, vcc, -1, v67, vcc
	global_load_dword v220, v[230:231], off
	s_mov_b32 s8, 0xfffd0000
	v_add_co_u32_e32 v230, vcc, s8, v66
	s_nop 1
	v_addc_co_u32_e32 v231, vcc, -1, v67, vcc
	global_load_dword v221, v[230:231], off
	s_mov_b32 s8, 0xfffd6000
	v_add_co_u32_e32 v230, vcc, s8, v66
	s_nop 1
	v_addc_co_u32_e32 v231, vcc, -1, v67, vcc
	global_load_dword v222, v[230:231], off
	s_mov_b32 s8, 0xfffdc000
	v_add_co_u32_e32 v230, vcc, s8, v66
	s_nop 1
	v_addc_co_u32_e32 v231, vcc, -1, v67, vcc
	global_load_dword v223, v[230:231], off
	s_mov_b32 s8, 0xfffe2000
	v_add_co_u32_e32 v230, vcc, s8, v66
	s_nop 1
	v_addc_co_u32_e32 v231, vcc, -1, v67, vcc
	global_load_dword v224, v[230:231], off
	s_mov_b32 s8, 0xfffe8000
	v_add_co_u32_e32 v230, vcc, s8, v66
	s_nop 1
	v_addc_co_u32_e32 v231, vcc, -1, v67, vcc
	global_load_dword v225, v[230:231], off
	s_mov_b32 s8, 0xfffee000
	v_add_co_u32_e32 v230, vcc, s8, v66
	s_nop 1
	v_addc_co_u32_e32 v231, vcc, -1, v67, vcc
	global_load_dword v226, v[230:231], off
	s_mov_b32 s8, 0xffff4000
	v_add_co_u32_e32 v230, vcc, s8, v66
	s_nop 1
	v_addc_co_u32_e32 v231, vcc, -1, v67, vcc
	global_load_dword v227, v[230:231], off
	s_mov_b32 s8, 0xffffa000
	v_add_co_u32_e32 v230, vcc, s8, v66
	s_nop 1
	v_addc_co_u32_e32 v231, vcc, -1, v67, vcc
	global_load_dword v228, v[230:231], off
	global_load_dword v229, v[66:67], off
	v_lshl_add_u64 v[66:67], v[66:67], 0, s[68:69]
.LBB0_26:
	s_waitcnt vmcnt(0)
	v_mov_b32_e32 v78, v214
	v_mov_b32_e32 v80, v215
	v_mov_b32_e32 v81, v216
	v_mov_b32_e32 v79, v217
	v_mov_b32_e32 v82, v218
	v_mov_b32_e32 v83, v219
	v_mov_b32_e32 v84, v220
	v_mov_b32_e32 v85, v221
	v_mov_b32_e32 v4, v222
	v_mov_b32_e32 v86, v223
	v_mov_b32_e32 v90, v224
	v_mov_b32_e32 v94, v225
	v_mov_b32_e32 v88, v226
	v_mov_b32_e32 v92, v227
	v_mov_b32_e32 v96, v228
	v_mov_b32_e32 v98, v229
	s_add_i32 s6, s6, 16
	s_cmpk_lt_u32 s6, 0xf0
	s_cbranch_scc0 .Lada_noissue
	s_mov_b32 s8, 0xfffa6000
	v_add_co_u32_e32 v230, vcc, s8, v66
	s_nop 1
	v_addc_co_u32_e32 v231, vcc, -1, v67, vcc
	global_load_dword v214, v[230:231], off
	s_mov_b32 s8, 0xfffac000
	v_add_co_u32_e32 v230, vcc, s8, v66
	s_nop 1
	v_addc_co_u32_e32 v231, vcc, -1, v67, vcc
	global_load_dword v215, v[230:231], off
	s_mov_b32 s8, 0xfffb2000
	v_add_co_u32_e32 v230, vcc, s8, v66
	s_nop 1
	v_addc_co_u32_e32 v231, vcc, -1, v67, vcc
	global_load_dword v216, v[230:231], off
	s_mov_b32 s8, 0xfffb8000
	v_add_co_u32_e32 v230, vcc, s8, v66
	s_nop 1
	v_addc_co_u32_e32 v231, vcc, -1, v67, vcc
	global_load_dword v217, v[230:231], off
	s_mov_b32 s8, 0xfffbe000
	v_add_co_u32_e32 v230, vcc, s8, v66
	s_nop 1
	v_addc_co_u32_e32 v231, vcc, -1, v67, vcc
	global_load_dword v218, v[230:231], off
	s_mov_b32 s8, 0xfffc4000
	v_add_co_u32_e32 v230, vcc, s8, v66
	s_nop 1
	v_addc_co_u32_e32 v231, vcc, -1, v67, vcc
	global_load_dword v219, v[230:231], off
	s_mov_b32 s8, 0xfffca000
	v_add_co_u32_e32 v230, vcc, s8, v66
	s_nop 1
	v_addc_co_u32_e32 v231, vcc, -1, v67, vcc
	global_load_dword v220, v[230:231], off
	s_mov_b32 s8, 0xfffd0000
	v_add_co_u32_e32 v230, vcc, s8, v66
	s_nop 1
	v_addc_co_u32_e32 v231, vcc, -1, v67, vcc
	global_load_dword v221, v[230:231], off
	s_mov_b32 s8, 0xfffd6000
	v_add_co_u32_e32 v230, vcc, s8, v66
	s_nop 1
	v_addc_co_u32_e32 v231, vcc, -1, v67, vcc
	global_load_dword v222, v[230:231], off
	s_mov_b32 s8, 0xfffdc000
	v_add_co_u32_e32 v230, vcc, s8, v66
	s_nop 1
	v_addc_co_u32_e32 v231, vcc, -1, v67, vcc
	global_load_dword v223, v[230:231], off
	s_mov_b32 s8, 0xfffe2000
	v_add_co_u32_e32 v230, vcc, s8, v66
	s_nop 1
	v_addc_co_u32_e32 v231, vcc, -1, v67, vcc
	global_load_dword v224, v[230:231], off
	s_mov_b32 s8, 0xfffe8000
	v_add_co_u32_e32 v230, vcc, s8, v66
	s_nop 1
	v_addc_co_u32_e32 v231, vcc, -1, v67, vcc
	global_load_dword v225, v[230:231], off
	s_mov_b32 s8, 0xfffee000
	v_add_co_u32_e32 v230, vcc, s8, v66
	s_nop 1
	v_addc_co_u32_e32 v231, vcc, -1, v67, vcc
	global_load_dword v226, v[230:231], off
	s_mov_b32 s8, 0xffff4000
	v_add_co_u32_e32 v230, vcc, s8, v66
	s_nop 1
	v_addc_co_u32_e32 v231, vcc, -1, v67, vcc
	global_load_dword v227, v[230:231], off
	s_mov_b32 s8, 0xffffa000
	v_add_co_u32_e32 v230, vcc, s8, v66
	s_nop 1
	v_addc_co_u32_e32 v231, vcc, -1, v67, vcc
	global_load_dword v228, v[230:231], off
	global_load_dword v229, v[66:67], off
	v_lshl_add_u64 v[66:67], v[66:67], 0, s[68:69]
.Lada_noissue:
	v_mov_b32_e32 v89, s7
	ds_read_b128 v[104:107], v89
	ds_read_b128 v[108:111], v89 offset:16
	ds_read_b128 v[112:115], v89 offset:32
	ds_read_b128 v[116:119], v89 offset:48
	ds_read_b128 v[120:123], v89 offset:4096
	ds_read_b128 v[124:127], v89 offset:8192
	ds_read_b128 v[128:131], v89 offset:12288
	ds_read_b128 v[132:135], v89 offset:16384
	ds_read_b128 v[136:139], v89 offset:20480
	ds_read_b128 v[140:143], v89 offset:24576
	ds_read_b128 v[144:147], v89 offset:28672
	ds_read_b128 v[148:151], v89 offset:32768
	s_add_i32 s7, s7, 64
	s_waitcnt lgkmcnt(0)
	v_mov_b32_e32 v152, v149
	v_mov_b32_e32 v149, v151
	v_mov_b32_e32 v153, v150
	v_pk_mul_f32 v[148:149], v[148:149], v[78:79]
	s_nop 0
	v_pk_fma_f32 v[212:213], v[152:153], v[80:81], v[148:149]
	ds_read_b128 v[148:151], v89 offset:4112
	ds_read_b128 v[152:155], v89 offset:8208
	ds_read_b128 v[156:159], v89 offset:12304
	ds_read_b128 v[160:163], v89 offset:16400
	ds_read_b128 v[164:167], v89 offset:20496
	ds_read_b128 v[168:171], v89 offset:24592
	ds_read_b128 v[172:175], v89 offset:28688
	ds_read_b128 v[176:179], v89 offset:32784
	ds_read_b128 v[180:183], v89 offset:4128
	ds_read_b128 v[184:187], v89 offset:8224
	ds_read_b128 v[188:191], v89 offset:12320
	ds_read_b128 v[192:195], v89 offset:16416
	ds_read_b128 v[196:199], v89 offset:20512
	ds_read_b128 v[200:203], v89 offset:24608
	ds_read_b128 v[204:207], v89 offset:28704
	ds_read_b128 v[208:211], v89 offset:32800
	s_waitcnt lgkmcnt(0)
	v_mul_f32_e32 v93, v208, v4
	v_mul_f32_e32 v208, v177, v83
	v_mul_f32_e32 v209, v209, v86
	v_pk_fma_f32 v[176:177], v[176:177], v[82:83], v[208:209] op_sel_hi:[1,1,0]
	v_mul_f32_e32 v208, v179, v85
	v_pk_fma_f32 v[178:179], v[178:179], v[84:85], v[208:209] op_sel_hi:[1,1,0]
	v_mov_b32_e32 v177, v93
	v_mov_b32_e32 v179, v209
	v_mul_f32_e32 v77, v210, v90
	v_pk_add_f32 v[176:177], v[176:177], v[178:179]
	v_pk_add_f32 v[178:179], v[212:213], v[212:213] op_sel:[0,1] op_sel_hi:[1,0]
	v_mul_f32_e32 v210, v211, v94
	v_mov_b32_e32 v179, v210
	v_pk_add_f32 v[76:77], v[76:77], v[178:179]
	v_mov_b32_e32 v210, v79
	v_pk_add_f32 v[208:209], v[176:177], v[76:77]
	v_mov_b32_e32 v77, v120
	v_mov_b32_e32 v120, v105
	v_mov_b32_e32 v76, v104
	v_pk_mul_f32 v[104:105], v[120:121], v[80:81] op_sel_hi:[1,0]
	v_mov_b32_e32 v120, v81
	v_pk_fma_f32 v[76:77], v[76:77], v[78:79], v[104:105] op_sel_hi:[1,0,1]
	v_mov_b32_e32 v105, v122
	v_mov_b32_e32 v122, v107
	v_mov_b32_e32 v104, v106
	v_pk_mul_f32 v[106:107], v[122:123], v[210:211] op_sel_hi:[1,0]
	v_mov_b32_e32 v122, v83
	v_pk_fma_f32 v[104:105], v[104:105], v[120:121], v[106:107] op_sel_hi:[1,0,1]
	ds_read_b128 v[176:179], v89 offset:4144
	v_pk_add_f32 v[76:77], v[76:77], v[104:105]
	s_nop 0
	v_pk_add_f32 v[70:71], v[70:71], v[76:77]
	v_mov_b32_e32 v77, v148
	v_mov_b32_e32 v148, v109
	v_mov_b32_e32 v76, v108
	v_pk_mul_f32 v[104:105], v[148:149], v[122:123] op_sel_hi:[1,0]
	v_mov_b32_e32 v148, v85
	v_pk_fma_f32 v[76:77], v[76:77], v[82:83], v[104:105] op_sel_hi:[1,0,1]
	v_mov_b32_e32 v105, v150
	v_mov_b32_e32 v150, v111
	v_mov_b32_e32 v104, v110
	v_pk_mul_f32 v[106:107], v[150:151], v[148:149] op_sel_hi:[1,0]
	s_nop 0
	v_pk_fma_f32 v[104:105], v[104:105], v[84:85], v[106:107] op_sel_hi:[1,0,1]
	s_nop 0
	v_pk_add_f32 v[76:77], v[76:77], v[104:105]
	s_nop 0
	v_pk_add_f32 v[70:71], v[70:71], v[76:77]
	v_mov_b32_e32 v77, v180
	v_mov_b32_e32 v180, v113
	v_mov_b32_e32 v76, v112
	v_pk_mul_f32 v[104:105], v[180:181], v[86:87] op_sel_hi:[1,0]
	s_nop 0
	v_pk_fma_f32 v[76:77], v[76:77], v[4:5], v[104:105] op_sel_hi:[1,0,1]
	v_mov_b32_e32 v105, v182
	v_mov_b32_e32 v182, v115
	v_mov_b32_e32 v104, v114
	v_pk_mul_f32 v[106:107], v[182:183], v[94:95] op_sel_hi:[1,0]
	s_nop 0
	v_pk_fma_f32 v[104:105], v[104:105], v[90:91], v[106:107] op_sel_hi:[1,0,1]
	s_nop 0
	v_pk_add_f32 v[76:77], v[76:77], v[104:105]
	s_nop 0
	v_pk_add_f32 v[70:71], v[70:71], v[76:77]
	s_waitcnt lgkmcnt(0)
	v_mov_b32_e32 v77, v176
	v_mov_b32_e32 v176, v117
	v_mov_b32_e32 v76, v116
	v_pk_mul_f32 v[104:105], v[176:177], v[92:93] op_sel_hi:[1,0]
	s_nop 0
	v_pk_fma_f32 v[76:77], v[76:77], v[88:89], v[104:105] op_sel_hi:[1,0,1]
	v_mov_b32_e32 v105, v178
	v_mov_b32_e32 v178, v119
	v_mov_b32_e32 v104, v118
	v_pk_mul_f32 v[106:107], v[178:179], v[98:99] op_sel_hi:[1,0]
	s_nop 0
	v_pk_fma_f32 v[104:105], v[104:105], v[96:97], v[106:107] op_sel_hi:[1,0,1]
	s_nop 0
	v_pk_add_f32 v[76:77], v[76:77], v[104:105]
	ds_read_b128 v[104:107], v89 offset:8240
	ds_read_b128 v[108:111], v89 offset:12336
	v_pk_add_f32 v[70:71], v[70:71], v[76:77]
	v_mov_b32_e32 v77, v128
	v_mov_b32_e32 v128, v125
	v_mov_b32_e32 v76, v124
	v_pk_mul_f32 v[112:113], v[128:129], v[80:81] op_sel_hi:[1,0]
	s_nop 0
	v_pk_fma_f32 v[76:77], v[76:77], v[78:79], v[112:113] op_sel_hi:[1,0,1]
	v_mov_b32_e32 v113, v130
	v_mov_b32_e32 v130, v127
	v_mov_b32_e32 v112, v126
	v_pk_mul_f32 v[114:115], v[130:131], v[210:211] op_sel_hi:[1,0]
	s_nop 0
	v_pk_fma_f32 v[112:113], v[112:113], v[120:121], v[114:115] op_sel_hi:[1,0,1]
	s_nop 0
	v_pk_add_f32 v[76:77], v[76:77], v[112:113]
	s_nop 0
	v_pk_add_f32 v[68:69], v[68:69], v[76:77]
	v_mov_b32_e32 v77, v156
	v_mov_b32_e32 v156, v153
	v_mov_b32_e32 v76, v152
	v_pk_mul_f32 v[112:113], v[156:157], v[122:123] op_sel_hi:[1,0]
	s_nop 0
	v_pk_fma_f32 v[76:77], v[76:77], v[82:83], v[112:113] op_sel_hi:[1,0,1]
	v_mov_b32_e32 v113, v158
	v_mov_b32_e32 v158, v155
	v_mov_b32_e32 v112, v154
	v_pk_mul_f32 v[114:115], v[158:159], v[148:149] op_sel_hi:[1,0]
	s_nop 0
	v_pk_fma_f32 v[112:113], v[112:113], v[84:85], v[114:115] op_sel_hi:[1,0,1]
	s_nop 0
	v_pk_add_f32 v[76:77], v[76:77], v[112:113]
	s_nop 0
	v_pk_add_f32 v[68:69], v[68:69], v[76:77]
	v_mov_b32_e32 v77, v188
	v_mov_b32_e32 v188, v185
	v_mov_b32_e32 v76, v184
	v_pk_mul_f32 v[112:113], v[188:189], v[86:87] op_sel_hi:[1,0]
	s_nop 0
	v_pk_fma_f32 v[76:77], v[76:77], v[4:5], v[112:113] op_sel_hi:[1,0,1]
	v_mov_b32_e32 v113, v190
	v_mov_b32_e32 v190, v187
	v_mov_b32_e32 v112, v186
	v_pk_mul_f32 v[114:115], v[190:191], v[94:95] op_sel_hi:[1,0]
	s_nop 0
	v_pk_fma_f32 v[112:113], v[112:113], v[90:91], v[114:115] op_sel_hi:[1,0,1]
	s_nop 0
	v_pk_add_f32 v[76:77], v[76:77], v[112:113]
	s_nop 0
	v_pk_add_f32 v[68:69], v[68:69], v[76:77]
	s_waitcnt lgkmcnt(0)
	v_mov_b32_e32 v77, v108
	v_mov_b32_e32 v108, v105
	v_mov_b32_e32 v76, v104
	v_pk_mul_f32 v[104:105], v[108:109], v[92:93] op_sel_hi:[1,0]
	s_nop 0
	v_pk_fma_f32 v[76:77], v[76:77], v[88:89], v[104:105] op_sel_hi:[1,0,1]
	v_mov_b32_e32 v105, v110
	v_mov_b32_e32 v110, v107
	v_mov_b32_e32 v104, v106
	v_pk_mul_f32 v[106:107], v[110:111], v[98:99] op_sel_hi:[1,0]
	s_nop 0
	v_pk_fma_f32 v[104:105], v[104:105], v[96:97], v[106:107] op_sel_hi:[1,0,1]
	s_nop 0
	v_pk_add_f32 v[76:77], v[76:77], v[104:105]
	ds_read_b128 v[104:107], v89 offset:16432
	ds_read_b128 v[108:111], v89 offset:20528
	v_pk_add_f32 v[68:69], v[68:69], v[76:77]
	v_mov_b32_e32 v77, v136
	v_mov_b32_e32 v136, v133
	v_mov_b32_e32 v76, v132
	v_pk_mul_f32 v[112:113], v[136:137], v[80:81] op_sel_hi:[1,0]
	s_nop 0
	v_pk_fma_f32 v[76:77], v[76:77], v[78:79], v[112:113] op_sel_hi:[1,0,1]
	v_mov_b32_e32 v113, v138
	v_mov_b32_e32 v138, v135
	v_mov_b32_e32 v112, v134
	v_pk_mul_f32 v[114:115], v[138:139], v[210:211] op_sel_hi:[1,0]
	s_nop 0
	v_pk_fma_f32 v[112:113], v[112:113], v[120:121], v[114:115] op_sel_hi:[1,0,1]
	s_nop 0
	v_pk_add_f32 v[76:77], v[76:77], v[112:113]
	s_nop 0
	v_pk_add_f32 v[72:73], v[72:73], v[76:77]
	v_mov_b32_e32 v77, v164
	v_mov_b32_e32 v164, v161
	v_mov_b32_e32 v76, v160
	v_pk_mul_f32 v[112:113], v[164:165], v[122:123] op_sel_hi:[1,0]
	s_nop 0
	v_pk_fma_f32 v[76:77], v[76:77], v[82:83], v[112:113] op_sel_hi:[1,0,1]
	v_mov_b32_e32 v113, v166
	v_mov_b32_e32 v166, v163
	v_mov_b32_e32 v112, v162
	v_pk_mul_f32 v[114:115], v[166:167], v[148:149] op_sel_hi:[1,0]
	s_nop 0
	v_pk_fma_f32 v[112:113], v[112:113], v[84:85], v[114:115] op_sel_hi:[1,0,1]
	s_nop 0
	v_pk_add_f32 v[76:77], v[76:77], v[112:113]
	s_nop 0
	v_pk_add_f32 v[72:73], v[72:73], v[76:77]
	v_mov_b32_e32 v77, v196
	v_mov_b32_e32 v196, v193
	v_mov_b32_e32 v76, v192
	v_pk_mul_f32 v[112:113], v[196:197], v[86:87] op_sel_hi:[1,0]
	s_nop 0
	v_pk_fma_f32 v[76:77], v[76:77], v[4:5], v[112:113] op_sel_hi:[1,0,1]
	v_mov_b32_e32 v113, v198
	v_mov_b32_e32 v198, v195
	v_mov_b32_e32 v112, v194
	v_pk_mul_f32 v[114:115], v[198:199], v[94:95] op_sel_hi:[1,0]
	s_nop 0
	v_pk_fma_f32 v[112:113], v[112:113], v[90:91], v[114:115] op_sel_hi:[1,0,1]
	s_nop 0
	v_pk_add_f32 v[76:77], v[76:77], v[112:113]
	s_nop 0
	v_pk_add_f32 v[72:73], v[72:73], v[76:77]
	s_waitcnt lgkmcnt(0)
	v_mov_b32_e32 v77, v108
	v_mov_b32_e32 v108, v105
	v_mov_b32_e32 v76, v104
	v_pk_mul_f32 v[104:105], v[108:109], v[92:93] op_sel_hi:[1,0]
	s_nop 0
	v_pk_fma_f32 v[76:77], v[76:77], v[88:89], v[104:105] op_sel_hi:[1,0,1]
	v_mov_b32_e32 v105, v110
	v_mov_b32_e32 v110, v107
	v_mov_b32_e32 v104, v106
	v_pk_mul_f32 v[106:107], v[110:111], v[98:99] op_sel_hi:[1,0]
	s_nop 0
	v_pk_fma_f32 v[104:105], v[104:105], v[96:97], v[106:107] op_sel_hi:[1,0,1]
	s_nop 0
	v_pk_add_f32 v[76:77], v[76:77], v[104:105]
	ds_read_b128 v[104:107], v89 offset:24624
	ds_read_b128 v[108:111], v89 offset:28720
	v_pk_add_f32 v[72:73], v[72:73], v[76:77]
	v_mov_b32_e32 v77, v144
	v_mov_b32_e32 v144, v141
	v_mov_b32_e32 v76, v140
	v_pk_mul_f32 v[80:81], v[144:145], v[80:81] op_sel_hi:[1,0]
	s_nop 0
	v_pk_fma_f32 v[76:77], v[76:77], v[78:79], v[80:81] op_sel_hi:[1,0,1]
	v_mov_b32_e32 v79, v146
	v_mov_b32_e32 v146, v143
	v_mov_b32_e32 v78, v142
	v_pk_mul_f32 v[80:81], v[146:147], v[210:211] op_sel_hi:[1,0]
	s_nop 0
	v_pk_fma_f32 v[78:79], v[78:79], v[120:121], v[80:81] op_sel_hi:[1,0,1]
	s_nop 0
	v_pk_add_f32 v[76:77], v[76:77], v[78:79]
	s_nop 0
	v_pk_add_f32 v[74:75], v[74:75], v[76:77]
	v_mov_b32_e32 v77, v172
	v_mov_b32_e32 v172, v169
	v_mov_b32_e32 v76, v168
	v_pk_mul_f32 v[78:79], v[172:173], v[122:123] op_sel_hi:[1,0]
	s_nop 0
	v_pk_fma_f32 v[76:77], v[76:77], v[82:83], v[78:79] op_sel_hi:[1,0,1]
	v_mov_b32_e32 v79, v174
	v_mov_b32_e32 v174, v171
	v_mov_b32_e32 v78, v170
	v_pk_mul_f32 v[80:81], v[174:175], v[148:149] op_sel_hi:[1,0]
	s_nop 0
	v_pk_fma_f32 v[78:79], v[78:79], v[84:85], v[80:81] op_sel_hi:[1,0,1]
	s_nop 0
	v_pk_add_f32 v[76:77], v[76:77], v[78:79]
	s_nop 0
	v_pk_add_f32 v[74:75], v[74:75], v[76:77]
	v_mov_b32_e32 v77, v204
	v_mov_b32_e32 v204, v201
	v_mov_b32_e32 v76, v200
	v_pk_mul_f32 v[78:79], v[204:205], v[86:87] op_sel_hi:[1,0]
	s_nop 0
	v_pk_fma_f32 v[76:77], v[76:77], v[4:5], v[78:79] op_sel_hi:[1,0,1]
	v_mov_b32_e32 v79, v206
	v_mov_b32_e32 v206, v203
	v_mov_b32_e32 v78, v202
	v_pk_mul_f32 v[80:81], v[206:207], v[94:95] op_sel_hi:[1,0]
	v_add_f32_e32 v4, v208, v209
	v_pk_fma_f32 v[78:79], v[78:79], v[90:91], v[80:81] op_sel_hi:[1,0,1]
	s_nop 0
	v_pk_add_f32 v[76:77], v[76:77], v[78:79]
	s_nop 0
	v_pk_add_f32 v[74:75], v[74:75], v[76:77]
	s_waitcnt lgkmcnt(0)
	v_mov_b32_e32 v77, v108
	v_mov_b32_e32 v108, v105
	v_mov_b32_e32 v76, v104
	v_pk_mul_f32 v[78:79], v[108:109], v[92:93] op_sel_hi:[1,0]
	v_mov_b32_e32 v93, v96
	v_pk_fma_f32 v[76:77], v[76:77], v[88:89], v[78:79] op_sel_hi:[1,0,1]
	v_mov_b32_e32 v79, v110
	v_mov_b32_e32 v110, v107
	v_mov_b32_e32 v78, v106
	v_pk_mul_f32 v[80:81], v[110:111], v[98:99] op_sel_hi:[1,0]
	s_nop 0
	v_pk_fma_f32 v[78:79], v[78:79], v[96:97], v[80:81] op_sel_hi:[1,0,1]
	s_nop 0
	v_pk_add_f32 v[76:77], v[76:77], v[78:79]
	s_nop 0
	v_pk_add_f32 v[74:75], v[74:75], v[76:77]
	ds_read_b128 v[76:79], v89 offset:32816
	v_mov_b32_e32 v89, v98
	s_waitcnt lgkmcnt(0)
	v_mov_b32_e32 v80, v77
	v_mov_b32_e32 v77, v79
	v_mov_b32_e32 v81, v78
	v_pk_mul_f32 v[76:77], v[76:77], v[88:89]
	s_nop 0
	v_pk_fma_f32 v[76:77], v[80:81], v[92:93], v[76:77]
	s_nop 0
	v_add_f32_e32 v76, v76, v77
	v_add_f32_e32 v76, v4, v76
	s_cmpk_lt_u32 s6, 0xf0
	s_cbranch_scc1 .LBB0_26
	ds_write2st64_b32 v103, v70, v71 offset1:2
	ds_write2st64_b32 v103, v68, v69 offset0:4 offset1:6
	ds_write2st64_b32 v103, v72, v73 offset0:8 offset1:10
	ds_write2st64_b32 v103, v74, v75 offset0:12 offset1:14
	ds_write_b32 v103, v76 offset:4096
	s_waitcnt lgkmcnt(0)
	s_barrier
	s_and_saveexec_b64 s[6:7], s[4:5]
	s_cbranch_execz .LBB0_30
	s_mul_i32 s8, s20, 0xffffffd0
	s_add_i32 s8, s8, s93
	s_lshl_b32 s22, s8, 7
	s_ashr_i32 s23, s22, 31
	s_lshl_b64 s[8:9], s[22:23], 2
	s_add_u32 s8, s16, s8
	s_addc_u32 s9, s34, s9
	s_add_i32 s74, s22, s21
	s_mul_hi_i32 s21, s20, 9
	s_mul_i32 s20, s20, 9
	s_mov_b64 s[22:23], 0
	v_mov_b32_e32 v66, v37
	v_mov_b32_e32 v67, v0
